# GEMM phases: static priority given to waves 0-3 instead of waves 4-7 (direction check of the static wave-half priority)
# baseline (speedup 1.0000x reference)
.LBB0_261:
	v_readlane_b32 s4, v255, 12
	v_readlane_b32 s5, v255, 13
	s_mov_b32 s5, s56
	v_writelane_b32 v255, s4, 12
	s_mov_b32 s22, s2
	v_mov_b32_e32 v11, v0
	v_writelane_b32 v255, s5, 13
	s_cmpk_gt_i32 s22, 0x76f
	v_readfirstlane_b32 s23, v11
	s_cbranch_scc1 .LBB0_273
	v_lshlrev_b32_e32 v2, 4, v11
	v_add_u32_e32 v3, 0x2000, v2
	v_ashrrev_i32_e32 v4, 31, v3
	v_lshrrev_b32_e32 v4, 22, v4
	v_add_u32_e32 v4, v3, v4
	v_ashrrev_i32_e32 v4, 10, v4
	v_mul_i32_i24_e32 v5, 0x400, v4
	v_sub_u32_e32 v3, v3, v5
	v_lshrrev_b32_e32 v5, 4, v3
	v_bitop3_b32 v3, v5, v3, 32 bitop3:0x6c
	v_ashrrev_i32_e32 v6, 31, v3
	v_lshrrev_b32_e32 v6, 26, v6
	v_add_u32_e32 v6, v3, v6
	v_ashrrev_i32_e32 v7, 6, v6
	v_and_b32_e32 v6, 0xc0, v6
	v_sub_u32_e32 v3, v3, v6
	v_bfe_i32 v6, v11, 27, 1
	v_lshrrev_b32_e32 v6, 22, v6
	v_add_u32_e32 v6, v2, v6
	v_and_b32_e32 v6, 0xfffffc00, v6
	v_sub_u32_e32 v2, v2, v6
	v_lshlrev_b32_e32 v5, 5, v4
	v_lshrrev_b32_e32 v6, 4, v2
	v_and_b32_e32 v5, 32, v5
	v_ashrrev_i16_sdwa v3, v1, sext(v3) dst_sel:DWORD dst_unused:UNUSED_PAD src0_sel:DWORD src1_sel:BYTE_0
	v_bitop3_b32 v6, v6, v2, 32 bitop3:0x6c
	v_ashrrev_i32_e32 v2, 31, v2
	v_add_u32_sdwa v10, v5, sext(v3) dst_sel:DWORD dst_unused:UNUSED_PAD src0_sel:DWORD src1_sel:WORD_0
	v_ashrrev_i32_e32 v3, 31, v11
	v_lshrrev_b32_e32 v2, 26, v2
	s_load_dwordx2 s[4:5], s[0:1], 0x258
	s_load_dwordx4 s[8:11], s[0:1], 0x130
	v_lshrrev_b32_e32 v3, 26, v3
	v_add_u32_e32 v2, v6, v2
	v_add_u32_e32 v3, v11, v3
	v_ashrrev_i32_e32 v2, 6, v2
	v_readlane_b32 s6, v255, 12
	v_ashrrev_i32_e32 v3, 6, v3
	v_mul_i32_i24_e32 v8, 64, v2
	s_mul_i32 s1, s6, 0x700000
	v_lshlrev_b32_e32 v5, 5, v3
	v_sub_u32_e32 v6, v6, v8
	v_lshlrev_b32_e32 v4, 3, v4
	v_lshlrev_b32_e32 v3, 3, v3
	s_mul_hi_u32 s0, s6, 0x700000
	s_waitcnt lgkmcnt(0)
	s_add_u32 s24, s4, s1
	v_and_b32_e32 v5, 32, v5
	v_ashrrev_i16_sdwa v6, v1, sext(v6) dst_sel:DWORD dst_unused:UNUSED_PAD src0_sel:DWORD src1_sel:BYTE_0
	v_and_b32_e32 v4, -16, v4
	v_and_b32_e32 v3, -16, v3
	s_addc_u32 s25, s5, s0
	v_add_u32_sdwa v5, v5, sext(v6) dst_sel:DWORD dst_unused:UNUSED_PAD src0_sel:DWORD src1_sel:WORD_0
	v_add_u32_e32 v4, v7, v4
	v_and_b32_e32 v6, 3, v7
	s_mov_b32 s0, 0x1fffe0
	v_add_u32_e32 v3, v2, v3
	v_and_b32_e32 v2, 3, v2
	s_ashr_i32 s27, s22, 31
	v_and_or_b32 v6, v4, s0, v6
	v_and_or_b32 v2, v3, s0, v2
	s_lshr_b32 s0, s27, 29
	s_add_i32 s0, s22, s0
	s_ashr_i32 s4, s23, 6
	s_ashr_i32 s5, s0, 3
	s_and_b32 s0, s0, -8
	s_ashr_i32 s1, s23, 8
	s_lshl_b32 s26, s4, 10
	s_sub_i32 s0, s22, s0
	s_cmp_lt_i32 s0, 0
	s_movk_i32 s6, 0xef
	s_cselect_b32 s6, s6, 0xee
	s_mul_i32 s0, s6, s0
	s_add_i32 s0, s0, s5
	s_mul_hi_i32 s5, s0, 0x92492493
	s_add_i32 s5, s5, s0
	s_lshr_b32 s6, s5, 31
	s_ashr_i32 s5, s5, 6
	s_add_i32 s5, s5, s6
	s_lshl_b32 s6, s5, 3
	s_mulk_i32 s5, 0x70
	s_sub_i32 s5, s0, s5
	s_bfe_i32 s0, s5, 0x80000
	v_readlane_b32 s7, v255, 13
	s_bfe_u32 s0, s0, 0x3000c
	v_lshrrev_b32_e32 v7, 2, v4
	v_lshlrev_b32_e32 v8, 1, v4
	s_add_i32 s7, s5, s0
	v_and_b32_e32 v7, 4, v7
	v_and_b32_e32 v8, 24, v8
	s_bfe_i32 s0, s7, 0x80000
	s_and_b32 s7, s7, 0xf8
	v_or3_b32 v6, v6, v7, v8
	v_lshlrev_b32_e32 v7, 1, v10
	s_sub_i32 s5, s5, s7
	v_lshl_add_u32 v130, v6, 11, v7
	v_lshrrev_b32_e32 v6, 2, v3
	v_lshlrev_b32_e32 v7, 1, v3
	s_sext_i32_i16 s0, s0
	s_sext_i32_i8 s5, s5
	v_and_b32_e32 v6, 4, v6
	v_and_b32_e32 v7, 24, v7
	s_lshr_b32 s0, s0, 3
	s_add_i32 s39, s6, s5
	v_or3_b32 v2, v2, v6, v7
	v_lshlrev_b32_e32 v6, 1, v5
	s_lshl_b32 s5, s39, 18
	v_lshl_add_u32 v146, v3, 10, v5
	v_lshlrev_b32_e32 v12, 10, v4
	s_bfe_i64 s[6:7], s[0:1], 0x100000
	v_lshl_add_u32 v132, v2, 11, v6
	v_add_lshl_u32 v134, v146, s5, 1
	v_add_u32_e32 v2, s5, v12
	s_bitset1_b32 s5, 17
	s_lshl_b64 s[6:7], s[6:7], 19
	s_add_u32 s16, s24, s6
	s_addc_u32 s17, s25, s7
	s_add_i32 s28, s26, 0
	s_add_i32 m0, s28, 0x10000
	s_add_i32 s29, s28, 0x2000
	global_load_lds_dwordx4 v132, s[16:17]
	s_add_i32 m0, s28, 0x12000
	v_add_lshl_u32 v136, v2, v10, 1
	global_load_lds_dwordx4 v130, s[16:17]
	s_mov_b32 m0, s28
	s_add_u32 s6, s16, 0x40000
	global_load_lds_dwordx4 v134, s[8:9]
	s_mov_b32 m0, s29
	s_addc_u32 s7, s17, 0
	global_load_lds_dwordx4 v136, s[8:9]
	s_add_i32 m0, s28, 0x14000
	s_add_i32 s30, s28, 0x4000
	global_load_lds_dwordx4 v132, s[6:7]
	s_add_i32 m0, s28, 0x16000
	v_add_lshl_u32 v138, v146, s5, 1
	v_add_u32_e32 v2, s5, v12
	global_load_lds_dwordx4 v130, s[6:7]
	s_mov_b32 m0, s30
	s_add_i32 s31, s28, 0x6000
	v_add_lshl_u32 v140, v2, v10, 1
	global_load_lds_dwordx4 v138, s[8:9]
	s_mov_b32 m0, s31
	v_mov_b32_e32 v133, v227
	global_load_lds_dwordx4 v140, s[8:9]
	v_mov_b32_e32 v131, v227
	v_mov_b32_e32 v135, v227
	v_mov_b32_e32 v137, v227
	v_lshl_add_u64 v[8:9], s[16:17], 0, v[132:133]
	v_lshl_add_u64 v[6:7], s[16:17], 0, v[130:131]
	v_lshl_add_u64 v[4:5], s[8:9], 0, v[134:135]
	s_setprio 1
	s_cmp_lg_u32 s1, 1
	v_lshl_add_u64 v[2:3], s[8:9], 0, v[136:137]
	s_cbranch_scc1 .LBB0_264
	s_barrier
	s_setprio 0

.LBB0_419:
	s_or_b64 exec, exec, s[0:1]
	s_mov_b64 s[4:5], s[72:73]
	s_mov_b32 s0, s2
	v_mov_b32_e32 v7, v0
	s_waitcnt lgkmcnt(0)
	s_barrier
	s_cmpk_gt_i32 s0, 0x3b7
	v_readfirstlane_b32 s16, v7
	s_cbranch_scc1 .LBB0_439
	v_bfe_i32 v4, v7, 27, 1
	v_lshlrev_b32_e32 v2, 4, v7
	v_lshrrev_b32_e32 v4, 22, v4
	v_add_u32_e32 v4, v2, v4
	v_and_b32_e32 v4, 0xfffffc00, v4
	v_ashrrev_i32_e32 v3, 31, v7
	v_sub_u32_e32 v4, v2, v4
	v_lshrrev_b32_e32 v3, 26, v3
	v_lshrrev_b32_e32 v5, 4, v4
	v_add_u32_e32 v3, v7, v3
	v_bitop3_b32 v5, v5, v4, 32 bitop3:0x6c
	v_ashrrev_i32_e32 v4, 31, v4
	v_ashrrev_i32_e32 v3, 6, v3
	v_lshrrev_b32_e32 v4, 26, v4
	v_lshlrev_b32_e32 v6, 3, v3
	v_add_u32_e32 v4, v5, v4
	v_and_b32_e32 v6, -16, v6
	v_ashrrev_i32_e32 v4, 6, v4
	v_add_u32_e32 v46, v4, v6
	v_mul_i32_i24_e32 v6, 64, v4
	v_lshlrev_b32_e32 v3, 5, v3
	v_sub_u32_e32 v5, v5, v6
	v_and_b32_e32 v3, 32, v3
	v_ashrrev_i16_sdwa v5, v1, sext(v5) dst_sel:DWORD dst_unused:UNUSED_PAD src0_sel:DWORD src1_sel:BYTE_0
	v_add_u32_e32 v2, 0x2000, v2
	v_add_u32_sdwa v47, v3, sext(v5) dst_sel:DWORD dst_unused:UNUSED_PAD src0_sel:DWORD src1_sel:WORD_0
	v_ashrrev_i32_e32 v3, 31, v2
	v_lshrrev_b32_e32 v3, 22, v3
	v_add_u32_e32 v3, v2, v3
	v_ashrrev_i32_e32 v3, 10, v3
	v_mul_i32_i24_e32 v5, 0x400, v3
	v_sub_u32_e32 v2, v2, v5
	v_lshrrev_b32_e32 v5, 4, v2
	v_bitop3_b32 v2, v5, v2, 32 bitop3:0x6c
	v_ashrrev_i32_e32 v6, 31, v2
	v_lshrrev_b32_e32 v6, 26, v6
	s_load_dwordx4 s[8:11], s[4:5], 0x1d0
	s_load_dwordx2 s[12:13], s[4:5], 0x1b0
	v_lshlrev_b32_e32 v5, 3, v3
	v_add_u32_e32 v6, v2, v6
	v_and_b32_e32 v5, -16, v5
	v_ashrrev_i32_e32 v8, 6, v6
	v_readlane_b32 s4, v255, 12
	v_add_u32_e32 v48, v8, v5
	v_and_b32_e32 v5, 0xc0, v6
	s_mul_hi_u32 s1, s4, 0x150000
	s_mul_i32 s4, s4, 0x150000
	v_lshlrev_b32_e32 v3, 5, v3
	v_sub_u32_e32 v2, v2, v5
	s_waitcnt lgkmcnt(0)
	s_add_u32 s17, s8, s4
	v_and_b32_e32 v3, 32, v3
	v_ashrrev_i16_sdwa v2, v1, sext(v2) dst_sel:DWORD dst_unused:UNUSED_PAD src0_sel:DWORD src1_sel:BYTE_0
	s_addc_u32 s18, s9, s1
	v_add_u32_sdwa v49, v3, sext(v2) dst_sel:DWORD dst_unused:UNUSED_PAD src0_sel:DWORD src1_sel:WORD_0
	v_and_b32_e32 v2, 3, v8
	s_mov_b32 s1, 0x1ffffe0
	v_lshrrev_b32_e32 v3, 2, v48
	v_lshlrev_b32_e32 v5, 1, v48
	v_and_or_b32 v2, v48, s1, v2
	v_and_b32_e32 v3, 4, v3
	v_and_b32_e32 v5, 24, v5
	v_or3_b32 v2, v2, v3, v5
	s_movk_i32 s20, 0x180
	v_mul_lo_u32 v2, v2, s20
	v_add_lshl_u32 v34, v2, v49, 1
	v_and_b32_e32 v2, 3, v4
	v_and_or_b32 v2, v46, s1, v2
	s_ashr_i32 s1, s0, 31
	s_lshr_b32 s6, s1, 29
	v_readlane_b32 s5, v255, 13
	s_add_i32 s6, s0, s6
	s_ashr_i32 s5, s16, 6
	s_ashr_i32 s7, s6, 3
	s_and_b32 s6, s6, -8
	s_ashr_i32 s4, s16, 8
	s_lshl_b32 s19, s5, 10
	s_sub_i32 s6, s0, s6
	s_cmp_lt_i32 s6, 0
	s_movk_i32 s8, 0x78
	s_cselect_b32 s8, s8, 0x77
	s_mul_i32 s6, s8, s6
	s_add_i32 s6, s6, s7
	s_mul_hi_i32 s7, s6, 0x92492493
	s_add_i32 s7, s7, s6
	s_lshr_b32 s8, s7, 31
	s_ashr_i32 s7, s7, 5
	s_add_i32 s7, s7, s8
	s_lshl_b32 s8, s7, 3
	s_mul_i32 s7, s7, 56
	s_sub_i32 s7, s6, s7
	s_bfe_i32 s6, s7, 0x80000
	s_bfe_u32 s6, s6, 0x3000c
	s_add_i32 s9, s7, s6
	s_bfe_i32 s6, s9, 0x80000
	s_and_b32 s9, s9, 0xf8
	s_sub_i32 s9, s7, s9
	s_sext_i32_i8 s9, s9
	s_sext_i32_i16 s14, s6
	s_add_i32 s30, s8, s9
	v_lshrrev_b32_e32 v3, 2, v46
	v_lshlrev_b32_e32 v4, 1, v46
	s_lshr_b32 s6, s14, 3
	s_lshl_b32 s15, s30, 8
	v_and_b32_e32 v3, 4, v3
	v_and_b32_e32 v4, 24, v4
	s_cmp_gt_i32 s7, 15
	v_or3_b32 v2, v2, v3, v4
	s_cselect_b64 s[8:9], -1, 0
	v_mul_lo_u32 v2, v2, s20
	s_and_b64 s[8:9], s[8:9], exec
	v_add_lshl_u32 v36, v2, v47, 1
	s_cselect_b32 s8, 0x80, 0
	v_add_u32_e32 v2, s15, v46
	v_mul_lo_u32 v2, v2, s20
	v_add_u32_e32 v3, s8, v47
	v_add_lshl_u32 v4, v2, v3, 1
	v_add_u32_e32 v2, s15, v48
	s_bitset1_b32 s15, 7
	v_add_u32_e32 v6, s15, v46
	v_mul_lo_u32 v6, v6, s20
	s_ashr_i32 s7, s14, 3
	v_add_lshl_u32 v226, v6, v3, 1
	v_add_u32_e32 v3, s15, v48
	s_mul_hi_i32 s15, s7, 0x18000
	s_mul_i32 s14, s7, 0x18000
	s_mov_b32 s9, s56
	v_add_u32_e32 v5, s8, v49
	s_or_b64 s[8:9], s[14:15], s[8:9]
	s_lshl_b64 s[8:9], s[8:9], 1
	s_add_u32 s14, s17, s8
	v_mul_lo_u32 v2, v2, s20
	v_mul_lo_u32 v3, v3, s20
	s_addc_u32 s15, s18, s9
	s_add_i32 s20, s19, 0
	s_add_i32 m0, s20, 0x10000
	s_add_i32 s21, s20, 0x2000
	global_load_lds_dwordx4 v36, s[14:15]
	s_add_i32 m0, s20, 0x12000
	v_add_lshl_u32 v2, v5, v2, 1
	global_load_lds_dwordx4 v34, s[14:15]
	s_mov_b32 m0, s20
	s_add_u32 s8, s14, 0x18000
	global_load_lds_dwordx4 v4, s[12:13]
	s_mov_b32 m0, s21
	s_addc_u32 s9, s15, 0
	global_load_lds_dwordx4 v2, s[12:13]
	s_add_i32 m0, s20, 0x14000
	s_add_i32 s22, s20, 0x4000
	global_load_lds_dwordx4 v36, s[8:9]
	s_add_i32 m0, s20, 0x16000
	s_add_i32 s23, s20, 0x6000
	global_load_lds_dwordx4 v34, s[8:9]
	s_mov_b32 m0, s22
	v_add_lshl_u32 v6, v3, v5, 1
	global_load_lds_dwordx4 v226, s[12:13]
	s_mov_b32 m0, s23
	v_mov_b32_e32 v37, v227
	global_load_lds_dwordx4 v6, s[12:13]
	v_mov_b32_e32 v35, v227
	v_mov_b32_e32 v5, v227
	v_mov_b32_e32 v3, v227
	s_movk_i32 s43, 0x180
	v_lshl_add_u64 v[14:15], s[14:15], 0, v[36:37]
	v_lshl_add_u64 v[12:13], s[14:15], 0, v[34:35]
	v_lshl_add_u64 v[10:11], s[12:13], 0, v[4:5]
	s_setprio 1
	s_cmp_lg_u32 s4, 1
	v_lshl_add_u64 v[8:9], s[12:13], 0, v[2:3]
	s_cbranch_scc1 .LBB0_422
	s_barrier
	s_setprio 0

.LBB0_981:
	v_mov_b32_e32 v10, v0
	s_cmp_ge_i32 s26, s12
	v_readfirstlane_b32 s27, v10
	s_cbranch_scc1 .LBB0_995
	v_lshlrev_b32_e32 v2, 4, v10
	v_add_u32_e32 v3, 0x2000, v2
	v_ashrrev_i32_e32 v4, 31, v3
	v_lshrrev_b32_e32 v4, 22, v4
	v_add_u32_e32 v4, v3, v4
	v_ashrrev_i32_e32 v4, 10, v4
	v_mul_i32_i24_e32 v6, 0x400, v4
	v_sub_u32_e32 v3, v3, v6
	v_lshrrev_b32_e32 v6, 4, v3
	v_bitop3_b32 v3, v6, v3, 32 bitop3:0x6c
	v_ashrrev_i32_e32 v6, 31, v3
	v_lshrrev_b32_e32 v6, 26, v6
	v_add_u32_e32 v6, v3, v6
	v_bfe_i32 v8, v10, 27, 1
	v_ashrrev_i32_e32 v7, 6, v6
	v_and_b32_e32 v6, 0xc0, v6
	v_lshrrev_b32_e32 v8, 22, v8
	v_lshlrev_b32_e32 v5, 5, v4
	v_sub_u32_e32 v3, v3, v6
	v_add_u32_e32 v8, v2, v8
	v_and_b32_e32 v5, 32, v5
	v_ashrrev_i16_sdwa v3, v1, sext(v3) dst_sel:DWORD dst_unused:UNUSED_PAD src0_sel:DWORD src1_sel:BYTE_0
	v_and_b32_e32 v8, 0xfffffc00, v8
	v_add_u32_sdwa v3, v5, sext(v3) dst_sel:DWORD dst_unused:UNUSED_PAD src0_sel:DWORD src1_sel:WORD_0
	v_ashrrev_i32_e32 v5, 31, v10
	v_sub_u32_e32 v2, v2, v8
	v_lshrrev_b32_e32 v5, 26, v5
	v_lshrrev_b32_e32 v8, 4, v2
	v_readlane_b32 s16, v255, 12
	v_add_u32_e32 v5, v10, v5
	v_bitop3_b32 v8, v8, v2, 32 bitop3:0x6c
	v_ashrrev_i32_e32 v2, 31, v2
	s_ashr_i32 s14, s27, 6
	v_readlane_b32 s17, v255, 13
	v_ashrrev_i32_e32 v5, 6, v5
	v_lshrrev_b32_e32 v2, 26, v2
	s_ashr_i32 s7, s27, 8
	s_lshl_b32 s28, s14, 10
	s_lshl_b64 s[16:17], s[16:17], 21
	v_lshlrev_b32_e32 v6, 5, v5
	v_add_u32_e32 v2, v8, v2
	v_lshlrev_b32_e32 v4, 3, v4
	v_lshlrev_b32_e32 v5, 3, v5
	s_waitcnt lgkmcnt(0)
	s_add_u32 s29, s0, s16
	v_ashrrev_i32_e32 v2, 6, v2
	v_and_b32_e32 v4, -16, v4
	v_and_b32_e32 v5, -16, v5
	s_addc_u32 s30, s1, s17
	v_mul_i32_i24_e32 v9, 64, v2
	v_add_u32_e32 v4, v7, v4
	v_and_b32_e32 v7, 3, v7
	s_mov_b32 s0, 0x1fffe0
	v_add_u32_e32 v5, v2, v5
	v_and_b32_e32 v2, 3, v2
	s_ashr_i32 s34, s26, 31
	v_and_or_b32 v7, v4, s0, v7
	v_and_or_b32 v2, v5, s0, v2
	s_lshr_b32 s0, s34, 29
	s_add_i32 s0, s26, s0
	s_lshr_b32 s31, s25, 1
	s_ashr_i32 s1, s0, 3
	s_and_b32 s0, s0, -8
	s_sub_i32 s0, s26, s0
	s_or_b32 s35, s31, 1
	s_cmp_lt_i32 s0, 0
	s_cselect_b32 s6, s35, s31
	s_mul_i32 s0, s6, s0
	s_add_i32 s0, s0, s1
	v_sub_u32_e32 v8, v8, v9
	s_ashr_i32 s1, s0, 31
	v_and_b32_e32 v6, 32, v6
	v_ashrrev_i16_sdwa v8, v1, sext(v8) dst_sel:DWORD dst_unused:UNUSED_PAD src0_sel:DWORD src1_sel:BYTE_0
	s_lshr_b32 s1, s1, 27
	v_add_u32_sdwa v6, v6, sext(v8) dst_sel:DWORD dst_unused:UNUSED_PAD src0_sel:DWORD src1_sel:WORD_0
	v_lshrrev_b32_e32 v8, 2, v4
	v_lshlrev_b32_e32 v9, 1, v4
	s_add_i32 s1, s0, s1
	v_and_b32_e32 v8, 4, v8
	v_and_b32_e32 v9, 24, v9
	s_ashr_i32 s6, s1, 5
	v_or3_b32 v7, v7, v8, v9
	v_lshlrev_b32_e32 v8, 1, v3
	s_lshl_b32 s15, s6, 3
	v_lshl_add_u32 v172, v7, 11, v8
	v_lshrrev_b32_e32 v7, 2, v5
	v_lshlrev_b32_e32 v8, 1, v5
	s_sub_i32 s6, s25, s15
	v_and_b32_e32 v7, 4, v7
	v_and_b32_e32 v8, 24, v8
	s_min_i32 s16, s6, 8
	v_or3_b32 v2, v2, v7, v8
	v_lshlrev_b32_e32 v7, 1, v6
	s_sext_i32_i8 s6, s16
	v_lshl_add_u32 v174, v2, 11, v7
	v_cvt_f32_i32_e32 v2, s6
	s_andn2_b32 s1, s1, 31
	s_sub_i32 s17, s0, s1
	v_cvt_f32_i32_e32 v7, s17
	v_rcp_iflag_f32_e32 v8, v2
	s_xor_b32 s0, s17, s6
	s_ashr_i32 s0, s0, 30
	s_or_b32 s6, s0, 1
	v_mul_f32_e32 v8, v7, v8
	v_trunc_f32_e32 v8, v8
	v_fma_f32 v7, -v8, v2, v7
	v_cvt_i32_f32_e32 v8, v8
	v_cmp_ge_f32_e64 s[0:1], |v7|, |v2|
	s_and_b64 s[0:1], s[0:1], exec
	s_cselect_b32 s0, s6, 0
	v_readfirstlane_b32 s1, v8
	s_add_i32 s6, s1, s0
	s_mul_i32 s0, s6, s16
	s_sub_i32 s0, s17, s0
	s_sext_i32_i8 s0, s0
	s_add_i32 s47, s15, s0
	s_lshl_b32 s0, s47, 18
	v_lshl_add_u32 v171, v5, 10, v6
	v_lshl_add_u32 v200, v4, 10, v3
	v_add_lshl_u32 v122, s0, v171, 1
	v_add_lshl_u32 v124, s0, v200, 1
	s_bitset1_b32 s0, 17
	v_add_lshl_u32 v128, s0, v171, 1
	v_add_lshl_u32 v126, s0, v200, 1
	s_bfe_i64 s[0:1], s[6:7], 0x80000
	s_lshl_b64 s[0:1], s[0:1], 19
	s_add_u32 s0, s29, s0
	s_addc_u32 s1, s30, s1
	s_add_i32 s36, s28, 0
	s_add_i32 m0, s36, 0x10000
	s_add_i32 s37, s36, 0x2000
	global_load_lds_dwordx4 v174, s[0:1]
	s_add_i32 m0, s36, 0x12000
	s_add_u32 s16, s0, 0x40000
	global_load_lds_dwordx4 v172, s[0:1]
	s_mov_b32 m0, s36
	s_addc_u32 s17, s1, 0
	global_load_lds_dwordx4 v122, s[8:9]
	s_mov_b32 m0, s37
	s_add_i32 s38, s36, 0x4000
	global_load_lds_dwordx4 v124, s[8:9]
	s_add_i32 m0, s36, 0x14000
	s_add_i32 s39, s36, 0x6000
	global_load_lds_dwordx4 v174, s[16:17]
	s_add_i32 m0, s36, 0x16000
	v_mov_b32_e32 v175, v227
	global_load_lds_dwordx4 v172, s[16:17]
	s_mov_b32 m0, s38
	v_mov_b32_e32 v173, v227
	global_load_lds_dwordx4 v128, s[8:9]
	s_mov_b32 m0, s39
	v_mov_b32_e32 v123, v227
	global_load_lds_dwordx4 v126, s[8:9]
	v_mov_b32_e32 v125, v227
	s_mov_b32 s13, s56
	v_lshl_add_u64 v[8:9], s[0:1], 0, v[174:175]
	v_lshl_add_u64 v[6:7], s[0:1], 0, v[172:173]
	v_lshl_add_u64 v[4:5], s[8:9], 0, v[122:123]
	s_setprio 1
	s_cmp_lg_u32 s7, 1
	v_lshl_add_u64 v[2:3], s[8:9], 0, v[124:125]
	s_cbranch_scc1 .LBB0_984
	s_barrier
	s_setprio 0

.LBB0_1230:
	v_mul_i32_i24_e32 v13, 64, v3
	v_sub_u32_e32 v6, v6, v13
	v_lshlrev_b32_e32 v5, 5, v5
	v_ashrrev_i16_sdwa v6, v1, sext(v6) dst_sel:DWORD dst_unused:UNUSED_PAD src0_sel:DWORD src1_sel:BYTE_0
	v_and_b32_e32 v5, 32, v5
	v_bfe_i32 v6, v6, 0, 16
	v_add_lshl_u32 v148, v5, v6, 1
	v_lshlrev_b32_e32 v6, 6, v4
	v_sub_u32_e32 v6, v8, v6
	v_lshlrev_b32_e32 v5, 5, v7
	v_ashrrev_i16_sdwa v6, v1, sext(v6) dst_sel:DWORD dst_unused:UNUSED_PAD src0_sel:DWORD src1_sel:BYTE_0
	v_and_b32_e32 v5, 32, v5
	v_bfe_i32 v6, v6, 0, 16
	v_add_lshl_u32 v149, v5, v6, 1
	v_lshlrev_b32_e32 v5, 1, v146
	v_lshrrev_b32_e32 v6, 2, v146
	v_and_b32_e32 v3, 3, v3
	s_mov_b32 s1, 0x1fffe0
	v_and_b32_e32 v5, 24, v5
	v_and_b32_e32 v6, 4, v6
	v_and_or_b32 v3, v146, s1, v3
	v_or3_b32 v3, v3, v6, v5
	v_lshl_add_u32 v130, v3, 11, v148
	v_lshlrev_b32_e32 v3, 1, v147
	v_lshrrev_b32_e32 v5, 2, v147
	v_and_b32_e32 v4, 3, v4
	v_and_b32_e32 v3, 24, v3
	v_and_b32_e32 v5, 4, v5
	v_and_or_b32 v4, v147, s1, v4
	v_or3_b32 v3, v4, v5, v3
	v_mov_b32_e32 v4, s6
	s_mov_b32 s9, s56
	v_readfirstlane_b32 s8, v4
	s_ashr_i32 s5, s27, 6
	s_ashr_i32 s1, s0, 31
	s_bfe_i64 s[8:9], s[8:9], 0x80000
	s_ashr_i32 s4, s27, 8
	s_lshl_b32 s30, s5, 10
	s_lshl_b64 s[8:9], s[8:9], 19
	s_lshl_b64 s[0:1], s[0:1], 22
	s_add_u32 s0, s12, s0
	s_addc_u32 s1, s13, s1
	s_add_u32 s0, s0, s8
	s_addc_u32 s1, s1, s9
	s_add_i32 s31, s30, 0
	s_add_i32 m0, s31, 0x10000
	v_lshl_add_u32 v132, v3, 11, v149
	global_load_lds_dwordx4 v130, s[0:1]
	s_add_i32 m0, s31, 0x12000
	s_waitcnt vmcnt(0)
	v_lshl_add_u32 v140, v9, 11, v148
	global_load_lds_dwordx4 v132, s[0:1]
	s_mov_b32 m0, s31
	s_add_i32 s34, s31, 0x2000
	v_lshl_add_u32 v138, v10, 11, v149
	global_load_lds_dwordx4 v140, s[10:11]
	s_mov_b32 m0, s34
	s_add_u32 s8, s0, 0x40000
	global_load_lds_dwordx4 v138, s[10:11]
	s_addc_u32 s9, s1, 0
	s_add_i32 m0, s31, 0x14000
	s_add_i32 s35, s31, 0x4000
	global_load_lds_dwordx4 v130, s[8:9]
	s_add_i32 m0, s31, 0x16000
	v_lshl_add_u32 v136, v11, 11, v148
	global_load_lds_dwordx4 v132, s[8:9]
	s_mov_b32 m0, s35
	s_add_i32 s36, s31, 0x6000
	v_lshl_add_u32 v134, v12, 11, v149
	global_load_lds_dwordx4 v136, s[10:11]
	s_mov_b32 m0, s36
	s_setprio 1
	s_cmp_lg_u32 s4, 1
	global_load_lds_dwordx4 v134, s[10:11]
	s_cbranch_scc1 .LBB0_1232
	s_barrier
	s_setprio 0

.LBB0_1315:
	v_bfe_i32 v4, v10, 27, 1
	v_lshlrev_b32_e32 v2, 4, v10
	v_lshrrev_b32_e32 v4, 22, v4
	v_add_u32_e32 v4, v2, v4
	v_and_b32_e32 v4, 0xfffffc00, v4
	v_sub_u32_e32 v4, v2, v4
	v_lshrrev_b32_e32 v5, 4, v4
	v_bitop3_b32 v5, v5, v4, 32 bitop3:0x6c
	v_ashrrev_i32_e32 v4, 31, v4
	v_ashrrev_i32_e32 v3, 31, v10
	v_lshrrev_b32_e32 v4, 26, v4
	v_lshrrev_b32_e32 v3, 26, v3
	v_add_u32_e32 v4, v5, v4
	v_add_u32_e32 v3, v10, v3
	v_ashrrev_i32_e32 v4, 6, v4
	v_ashrrev_i32_e32 v3, 6, v3
	v_mul_i32_i24_e32 v7, 64, v4
	v_lshlrev_b32_e32 v6, 3, v3
	v_lshlrev_b32_e32 v3, 5, v3
	v_sub_u32_e32 v5, v5, v7
	v_and_b32_e32 v3, 32, v3
	v_ashrrev_i16_sdwa v5, v1, sext(v5) dst_sel:DWORD dst_unused:UNUSED_PAD src0_sel:DWORD src1_sel:BYTE_0
	v_add_u32_e32 v2, 0x2000, v2
	v_add_u32_sdwa v3, v3, sext(v5) dst_sel:DWORD dst_unused:UNUSED_PAD src0_sel:DWORD src1_sel:WORD_0
	v_ashrrev_i32_e32 v5, 31, v2
	v_lshrrev_b32_e32 v5, 22, v5
	v_add_u32_e32 v5, v2, v5
	v_ashrrev_i32_e32 v5, 10, v5
	v_mul_i32_i24_e32 v7, 0x400, v5
	v_sub_u32_e32 v2, v2, v7
	v_lshrrev_b32_e32 v7, 4, v2
	v_bitop3_b32 v2, v7, v2, 32 bitop3:0x6c
	v_ashrrev_i32_e32 v8, 31, v2
	v_lshrrev_b32_e32 v8, 26, v8
	v_add_u32_e32 v8, v2, v8
	v_ashrrev_i32_e32 v9, 6, v8
	v_and_b32_e32 v8, 0xc0, v8
	v_lshlrev_b32_e32 v7, 3, v5
	v_lshlrev_b32_e32 v5, 5, v5
	v_sub_u32_e32 v2, v2, v8
	v_and_b32_e32 v6, -16, v6
	v_and_b32_e32 v7, -16, v7
	v_and_b32_e32 v5, 32, v5
	v_ashrrev_i16_sdwa v2, v1, sext(v2) dst_sel:DWORD dst_unused:UNUSED_PAD src0_sel:DWORD src1_sel:BYTE_0
	v_add_u32_e32 v6, v4, v6
	v_add_u32_e32 v7, v9, v7
	v_add_u32_sdwa v2, v5, sext(v2) dst_sel:DWORD dst_unused:UNUSED_PAD src0_sel:DWORD src1_sel:WORD_0
	s_lshl_b32 s1, s46, 18
	v_lshl_add_u32 v146, v6, 10, v3
	v_lshl_add_u32 v147, v7, 10, v2
	v_add_lshl_u32 v134, s1, v146, 1
	v_add_lshl_u32 v136, s1, v147, 1
	s_bitset1_b32 s1, 17
	v_add_lshl_u32 v140, s1, v146, 1
	v_add_lshl_u32 v138, s1, v147, 1
	v_lshlrev_b32_e32 v5, 1, v6
	v_lshrrev_b32_e32 v8, 2, v6
	v_and_b32_e32 v4, 3, v4
	s_mov_b32 s1, 0x1fffe0
	v_and_b32_e32 v5, 24, v5
	v_and_b32_e32 v8, 4, v8
	v_and_or_b32 v4, v6, s1, v4
	v_or3_b32 v4, v4, v8, v5
	v_lshlrev_b32_e32 v3, 1, v3
	v_lshl_add_u32 v130, v4, 11, v3
	v_lshlrev_b32_e32 v3, 1, v7
	v_lshrrev_b32_e32 v4, 2, v7
	v_and_b32_e32 v5, 3, v9
	v_and_b32_e32 v3, 24, v3
	v_and_b32_e32 v4, 4, v4
	v_and_or_b32 v5, v7, s1, v5
	v_or3_b32 v3, v5, v4, v3
	v_lshlrev_b32_e32 v2, 1, v2
	v_lshl_add_u32 v132, v3, 11, v2
	v_mov_b32_e32 v2, s6
	s_mov_b32 s19, s56
	v_readfirstlane_b32 s18, v2
	s_ashr_i32 s5, s30, 6
	s_ashr_i32 s1, s0, 31
	s_bfe_i64 s[18:19], s[18:19], 0x80000
	s_ashr_i32 s4, s30, 8
	s_lshl_b32 s36, s5, 10
	s_lshl_b64 s[18:19], s[18:19], 19
	s_lshl_b64 s[0:1], s[0:1], 21
	s_waitcnt lgkmcnt(0)
	s_add_u32 s0, s14, s0
	s_addc_u32 s1, s15, s1
	s_add_u32 s22, s0, s18
	s_addc_u32 s23, s1, s19
	s_add_i32 s37, s36, 0
	s_add_i32 m0, s37, 0x10000
	s_add_i32 s38, s37, 0x2000
	global_load_lds_dwordx4 v130, s[22:23]
	s_add_i32 m0, s37, 0x12000
	s_add_u32 s0, s22, 0x40000
	global_load_lds_dwordx4 v132, s[22:23]
	s_mov_b32 m0, s37
	s_addc_u32 s1, s23, 0
	global_load_lds_dwordx4 v134, s[8:9]
	s_mov_b32 m0, s38
	s_add_i32 s39, s37, 0x4000
	global_load_lds_dwordx4 v136, s[8:9]
	s_add_i32 m0, s37, 0x14000
	s_add_i32 s40, s37, 0x6000
	global_load_lds_dwordx4 v130, s[0:1]
	s_add_i32 m0, s37, 0x16000
	v_mov_b32_e32 v131, v227
	global_load_lds_dwordx4 v132, s[0:1]
	s_mov_b32 m0, s39
	v_mov_b32_e32 v133, v227
	global_load_lds_dwordx4 v140, s[8:9]
	s_mov_b32 m0, s40
	v_mov_b32_e32 v135, v227
	global_load_lds_dwordx4 v138, s[8:9]
	v_mov_b32_e32 v137, v227
	v_lshl_add_u64 v[8:9], s[22:23], 0, v[130:131]
	v_lshl_add_u64 v[6:7], s[22:23], 0, v[132:133]
	v_lshl_add_u64 v[4:5], s[8:9], 0, v[134:135]
	s_setprio 1
	s_cmp_lg_u32 s4, 1
	v_lshl_add_u64 v[2:3], s[8:9], 0, v[136:137]
	s_cbranch_scc1 .LBB0_1317
	s_barrier
	s_setprio 0
